# dilated-attention units claimed from per-XCD queues (each XCD owns a contiguous range of unit indices, adjacent query blocks of a head share K/V tiles in that XCD's L2)
# baseline (speedup 1.0000x reference)
; #define LAS __attribute__((address_space(3)))
; __device__ __forceinline__ void at_dil(const Args& a, LAS unsigned char* lds, int layer) {
;     ...
;     unsigned* queue = (unsigned*)(a.ws + WS_CTL) + CW_QUEUE + (layer + 4) * 64;
;     LAS int* info = (LAS int*)(lds + L_INFO);
;     LAS float* tab = (LAS float*)(lds + L_TAB);
;     LAS float* relb = (LAS float*)(lds + SEG_OFF + 256);
;     float bdil, bmax;
;     { const int l64 = tid & 63;
;       float g2 = fabsf(a.in[I_QGD][layer * 64 + l64]), g3 = fabsf(a.in[I_KGD][layer * 64 + l64]);
;       float rbm = 0.f;
;       for (int i = l64; i < 32 * 6; i += 64) rbm = fmaxf(rbm, a.in[I_RELB][i]);
; #pragma unroll
;       for (int o2 = 1; o2 < 64; o2 <<= 1) { g2 = fmaxf(g2, __shfl_xor(g2, o2)); g3 = fmaxf(g3, __shfl_xor(g3, o2)); rbm = fmaxf(rbm, __shfl_xor(rbm, o2)); }
;       bdil = 8.f * g2 * g3 * LOG2E * 1.01f; bmax = fmaxf(rbm, 0.f) * LOG2E; }
;     const bool dil_fixed = (bdil + bmax) < 40.f;
;     const float m_dil = bdil + bmax;
;     const unsigned l0 = (unsigned)(uintptr_t)lds;
;     __syncthreads();
;     if (tid < 32 * 6) relb[tid] = a.in[I_RELB][tid] * LOG2E;
;     if (tid == 0) info[1] = (int)__hip_atomic_fetch_add(queue, 2u, __ATOMIC_RELAXED, __HIP_MEMORY_SCOPE_AGENT);
.LBB0_530:
	s_or_b64 exec, exec, s[4:5]
	s_lshl_b64 s[4:5], s[34:35], 2
	s_add_u32 s2, s92, s4
	s_addc_u32 s4, s93, s5
	s_add_u32 s12, s2, 0x14400
	s_addc_u32 s13, s4, 0
	s_and_b32 vcc_lo, s61, 7
	s_lshl_b32 vcc_lo, vcc_lo, 9
	s_addk_i32 vcc_lo, 0x2000
	s_add_u32 s12, s12, vcc_lo
	s_addc_u32 s13, s13, 0
	v_cmp_eq_u32_e64 s[4:5], 0, v18
	s_and_saveexec_b64 s[6:7], s[4:5]
	s_cbranch_execz .LBB0_534
	s_mov_b64 s[10:11], exec
	v_mbcnt_lo_u32_b32 v8, s10, 0
	v_mbcnt_hi_u32_b32 v8, s11, v8
	v_cmp_eq_u32_e32 vcc, 0, v8
	s_and_saveexec_b64 s[8:9], vcc
	s_cbranch_execz .LBB0_533
	s_bcnt1_i32_b64 s2, s[10:11]
	s_lshl_b32 s2, s2, 1
	v_mov_b32_e32 v9, s2
	global_atomic_add v9, v35, v9, s[12:13] sc0
.LBB0_533:
	s_or_b64 exec, exec, s[8:9]
	s_waitcnt vmcnt(0)
	v_readfirstlane_b32 s2, v9
	s_and_b32 vcc_lo, s61, 7
	s_mulk_i32 vcc_lo, 0x120
	s_cmpk_lt_u32 s2, 0x120
	s_cselect_b32 vcc_lo, vcc_lo, 0x900
	s_add_u32 s2, s2, vcc_lo
	s_nop 1
	v_lshl_add_u32 v8, v8, 1, s2
	v_readlane_b32 s2, v253, 55
	s_nop 1
	v_mov_b32_e32 v9, s2
	ds_write_b32 v9, v8

; __device__ __forceinline__ void at_dil(const Args& a, LAS unsigned char* lds, int layer) {
;     ...
;         unsigned nextu = 0;
;         if (tid == 0) nextu = __hip_atomic_fetch_add(queue, 1u, __ATOMIC_RELAXED, __HIP_MEMORY_SCOPE_AGENT);
;         const int twlo = wid >> 1;
;     ...
;         if (tid == 0) info[1] = (int)nextu;
;         asm volatile("s_waitcnt vmcnt(0) lgkmcnt(0)\n\ts_barrier" ::: "memory");
;         const int un2 = info[1];
.LBB0_556:
	s_or_b64 exec, exec, s[22:23]
	s_waitcnt vmcnt(0)
	v_readfirstlane_b32 s22, v19
	s_and_b32 vcc_lo, s61, 7
	s_mulk_i32 vcc_lo, 0x120
	s_cmpk_lt_u32 s22, 0x120
	s_cselect_b32 vcc_lo, vcc_lo, 0x900
	s_add_u32 s22, s22, vcc_lo
	s_nop 1
	v_add_u32_e32 v34, s22, v18
